# P8 finish0 row loop: all fourteen row loads requested at the top of the iteration (memory-level parallelism), counted waits re-derived
# baseline (speedup 1.0000x reference)
.LBB0_1118:
	v_lshl_add_u64 v[40:41], s[12:13], 0, v[34:35]
	v_add_co_u32_e64 v40, s[2:3], s5, v40
	v_lshl_add_u64 v[38:39], s[16:17], 0, v[34:35]
	s_nop 0
	v_addc_co_u32_e64 v41, s[2:3], 0, v41, s[2:3]
	v_add_co_u32_e64 v48, s[2:3], s7, v38
	v_lshl_add_u64 v[36:37], s[8:9], 0, v[34:35]
	v_add_co_u32_e32 v70, vcc, 0x3ac00000, v38
	v_addc_co_u32_e64 v49, s[2:3], 0, v39, s[2:3]
	v_add_co_u32_e64 v44, s[2:3], s30, v36
	v_addc_co_u32_e32 v71, vcc, 0, v39, vcc
	s_nop 0
	v_addc_co_u32_e64 v45, s[2:3], 0, v37, s[2:3]
	v_add_co_u32_e32 v72, vcc, 0x70600000, v36
	v_add_co_u32_e64 v52, s[2:3], s31, v36
	global_load_dwordx4 v[62:65], v[70:71], off offset:2048
	v_addc_co_u32_e32 v73, vcc, 0, v37, vcc
	v_addc_co_u32_e64 v53, s[2:3], 0, v37, s[2:3]
	v_add_co_u32_e32 v74, vcc, 0x74800000, v36
	v_add_co_u32_e64 v56, s[2:3], s35, v36
	s_nop 0
	v_addc_co_u32_e32 v75, vcc, 0, v37, vcc
	v_lshl_add_u64 v[46:47], v[38:39], 0, s[20:21]
	v_lshl_add_u64 v[42:43], v[36:37], 0, s[22:23]
	v_lshl_add_u64 v[50:51], v[36:37], 0, s[24:25]
	v_lshl_add_u64 v[54:55], v[36:37], 0, s[28:29]
	v_addc_co_u32_e64 v57, s[2:3], 0, v37, s[2:3]
	global_load_dwordx4 v[66:69], v[72:73], off
	global_load_dwordx4 v[36:39], v[74:75], off
	global_load_dwordx4 v[112:115], v[70:71], off offset:2064
	global_load_dwordx4 v[116:119], v[72:73], off offset:16
	global_load_dwordx4 v[120:123], v[74:75], off offset:16
	global_load_dwordx4 v[124:127], v[48:49], off offset:2048
	global_load_dwordx4 v[128:131], v[46:47], off offset:16
	global_load_dwordx4 v[132:135], v[42:43], off offset:16
	global_load_dwordx4 v[136:139], v[50:51], off offset:16
	global_load_dwordx4 v[140:143], v[44:45], off
	global_load_dwordx4 v[144:147], v[52:53], off
	global_load_dwordx4 v[148:151], v[56:57], off
	global_load_dwordx4 v[152:155], v[54:55], off offset:16
	s_add_i32 s4, s4, s6
	s_add_u32 s8, s8, s10
	s_addc_u32 s9, s9, s11
	s_add_u32 s12, s12, s14
	s_addc_u32 s13, s13, s15
	s_add_u32 s16, s16, s18
	s_addc_u32 s17, s17, s19
	s_cmp_lt_i32 s4, 0x8400
	s_waitcnt vmcnt(11)
	v_lshlrev_b32_e32 v76, 16, v62
	v_and_b32_e32 v77, 0xffff0000, v62
	v_lshlrev_b32_e32 v62, 16, v63
	v_and_b32_e32 v63, 0xffff0000, v63
	v_lshlrev_b32_e32 v78, 16, v64
	v_and_b32_e32 v79, 0xffff0000, v64
	v_lshlrev_b32_e32 v64, 16, v65
	v_and_b32_e32 v65, 0xffff0000, v65
	v_mul_f32_e32 v94, 0x3d372713, v76
	v_mul_f32_e32 v96, 0x3d372713, v77
	v_mul_f32_e32 v98, 0x3d372713, v62
	v_mul_f32_e32 v100, 0x3d372713, v63
	v_mul_f32_e32 v102, 0x3d372713, v78
	v_mul_f32_e32 v104, 0x3d372713, v79
	v_mul_f32_e32 v106, 0x3d372713, v64
	v_mul_f32_e32 v108, 0x3d372713, v65
	v_mov_b32_e32 v95, v76
	v_mov_b32_e32 v97, v77
	v_pk_mul_f32 v[82:83], v[76:77], 0.5 op_sel_hi:[1,0]
	v_mov_b32_e32 v99, v62
	v_mov_b32_e32 v101, v63
	v_mov_b32_e32 v103, v78
	v_mov_b32_e32 v105, v79
	v_pk_mul_f32 v[88:89], v[78:79], 0.5 op_sel_hi:[1,0]
	v_mov_b32_e32 v107, v64
	v_mov_b32_e32 v109, v65
	v_mul_f32_e32 v76, v94, v76
	v_mul_f32_e32 v77, v96, v77
	v_mul_f32_e32 v94, v98, v62
	v_mul_f32_e32 v96, v100, v63
	v_mul_f32_e32 v78, v102, v78
	v_mul_f32_e32 v79, v104, v79
	v_mul_f32_e32 v98, v106, v64
	v_mul_f32_e32 v100, v108, v65
	v_lshlrev_b32_e32 v80, 16, v66
	v_and_b32_e32 v81, 0xffff0000, v66
	v_lshlrev_b32_e32 v66, 16, v67
	v_and_b32_e32 v67, 0xffff0000, v67
	v_pk_mul_f32 v[84:85], v[62:63], 0.5 op_sel_hi:[1,0]
	v_lshlrev_b32_e32 v86, 16, v68
	v_and_b32_e32 v87, 0xffff0000, v68
	v_lshlrev_b32_e32 v68, 16, v69
	v_and_b32_e32 v69, 0xffff0000, v69
	v_lshlrev_b32_e32 v92, 16, v36
	v_and_b32_e32 v93, 0xffff0000, v36
	v_lshlrev_b32_e32 v36, 16, v37
	v_and_b32_e32 v37, 0xffff0000, v37
	v_lshlrev_b32_e32 v62, 16, v38
	v_and_b32_e32 v63, 0xffff0000, v38
	v_lshlrev_b32_e32 v38, 16, v39
	v_and_b32_e32 v39, 0xffff0000, v39
	v_fmac_f32_e32 v95, v76, v95
	v_fmac_f32_e32 v97, v77, v97
	v_fmac_f32_e32 v99, v94, v99
	v_fmac_f32_e32 v101, v96, v101
	v_fmac_f32_e32 v103, v78, v103
	v_fmac_f32_e32 v105, v79, v105
	v_fmac_f32_e32 v107, v98, v107
	v_fmac_f32_e32 v109, v100, v109
	v_pk_add_f32 v[36:37], v[66:67], v[36:37]
	v_pk_add_f32 v[38:39], v[68:69], v[38:39]
	v_mul_f32_e32 v66, 0x3f4c422a, v95
	v_mul_f32_e32 v67, 0x3f4c422a, v97
	v_mul_f32_e32 v68, 0x3f4c422a, v99
	v_mul_f32_e32 v69, 0x3f4c422a, v101
	v_mul_f32_e32 v76, 0x3f4c422a, v103
	v_mul_f32_e32 v77, 0x3f4c422a, v105
	v_mul_f32_e32 v78, 0x3f4c422a, v107
	v_mul_f32_e32 v79, 0x3f4c422a, v109
	v_add_f32_e32 v66, v66, v66
	v_add_f32_e32 v67, v67, v67
	v_add_f32_e32 v68, v68, v68
	v_add_f32_e32 v69, v69, v69
	v_add_f32_e32 v76, v76, v76
	v_add_f32_e32 v77, v77, v77
	v_add_f32_e32 v78, v78, v78
	v_add_f32_e32 v79, v79, v79
	v_mul_f32_e32 v66, 0x3fb8aa3b, v66
	v_mul_f32_e32 v67, 0x3fb8aa3b, v67
	v_mul_f32_e32 v68, 0x3fb8aa3b, v68
	v_mul_f32_e32 v69, 0x3fb8aa3b, v69
	v_mul_f32_e32 v76, 0x3fb8aa3b, v76
	v_mul_f32_e32 v77, 0x3fb8aa3b, v77
	v_mul_f32_e32 v78, 0x3fb8aa3b, v78
	v_mul_f32_e32 v79, 0x3fb8aa3b, v79
	v_exp_f32_e32 v66, v66
	v_exp_f32_e32 v67, v67
	v_exp_f32_e32 v68, v68
	v_exp_f32_e32 v69, v69
	v_exp_f32_e32 v76, v76
	v_exp_f32_e32 v77, v77
	v_exp_f32_e32 v78, v78
	v_exp_f32_e32 v79, v79
	v_add_f32_e32 v66, 1.0, v66
	v_add_f32_e32 v67, 1.0, v67
	v_add_f32_e32 v68, 1.0, v68
	v_add_f32_e32 v69, 1.0, v69
	v_add_f32_e32 v76, 1.0, v76
	v_add_f32_e32 v77, 1.0, v77
	v_add_f32_e32 v78, 1.0, v78
	v_add_f32_e32 v79, 1.0, v79
	v_rcp_f32_e32 v66, v66
	v_rcp_f32_e32 v67, v67
	v_rcp_f32_e32 v68, v68
	v_rcp_f32_e32 v69, v69
	v_rcp_f32_e32 v76, v76
	v_rcp_f32_e32 v77, v77
	v_rcp_f32_e32 v78, v78
	v_rcp_f32_e32 v79, v79
	v_pk_fma_f32 v[66:67], v[66:67], 2.0, 1.0 op_sel_hi:[1,0,0] neg_lo:[1,0,0] neg_hi:[1,0,0]
	v_pk_fma_f32 v[68:69], v[68:69], 2.0, 1.0 op_sel_hi:[1,0,0] neg_lo:[1,0,0] neg_hi:[1,0,0]
	v_pk_fma_f32 v[76:77], v[76:77], 2.0, 1.0 op_sel_hi:[1,0,0] neg_lo:[1,0,0] neg_hi:[1,0,0]
	v_pk_fma_f32 v[78:79], v[78:79], 2.0, 1.0 op_sel_hi:[1,0,0] neg_lo:[1,0,0] neg_hi:[1,0,0]
	v_pk_mul_f32 v[90:91], v[64:65], 0.5 op_sel_hi:[1,0]
	v_pk_add_f32 v[66:67], v[66:67], 1.0 op_sel_hi:[1,0]
	v_pk_add_f32 v[68:69], v[68:69], 1.0 op_sel_hi:[1,0]
	v_pk_add_f32 v[76:77], v[76:77], 1.0 op_sel_hi:[1,0]
	v_pk_add_f32 v[78:79], v[78:79], 1.0 op_sel_hi:[1,0]
	v_pk_add_f32 v[64:65], v[80:81], v[92:93]
	v_pk_add_f32 v[62:63], v[86:87], v[62:63]
	v_pk_mul_f32 v[66:67], v[82:83], v[66:67]
	v_pk_mul_f32 v[68:69], v[84:85], v[68:69]
	v_pk_mul_f32 v[76:77], v[88:89], v[76:77]
	v_pk_mul_f32 v[78:79], v[90:91], v[78:79]
	v_pk_mul_f32 v[64:65], v[64:65], v[66:67]
	v_pk_mul_f32 v[66:67], v[36:37], v[68:69]
	v_pk_mul_f32 v[62:63], v[62:63], v[76:77]
	v_pk_mul_f32 v[68:69], v[38:39], v[78:79]
	v_cvt_pk_bf16_f32 v36, v64, v65
	v_cvt_pk_bf16_f32 v37, v66, v67
	v_cvt_pk_bf16_f32 v38, v62, v63
	v_cvt_pk_bf16_f32 v39, v68, v69
	global_store_dwordx4 v[40:41], v[36:39], off
	s_waitcnt vmcnt(11)
	v_lshlrev_b32_e32 v70, 16, v112
	v_and_b32_e32 v71, 0xffff0000, v112
	v_lshlrev_b32_e32 v36, 16, v113
	v_and_b32_e32 v37, 0xffff0000, v113
	v_lshlrev_b32_e32 v76, 16, v114
	v_and_b32_e32 v77, 0xffff0000, v114
	v_lshlrev_b32_e32 v38, 16, v115
	v_and_b32_e32 v39, 0xffff0000, v115
	s_waitcnt vmcnt(10)
	v_lshlrev_b32_e32 v72, 16, v116
	v_and_b32_e32 v73, 0xffff0000, v116
	s_waitcnt vmcnt(9)
	v_lshlrev_b32_e32 v74, 16, v120
	v_and_b32_e32 v75, 0xffff0000, v120
	v_lshlrev_b32_e32 v78, 16, v118
	v_and_b32_e32 v79, 0xffff0000, v118
	v_lshlrev_b32_e32 v80, 16, v122
	v_and_b32_e32 v81, 0xffff0000, v122
	v_lshlrev_b32_e32 v64, 16, v119
	v_and_b32_e32 v65, 0xffff0000, v119
	v_lshlrev_b32_e32 v68, 16, v123
	v_and_b32_e32 v69, 0xffff0000, v123
	v_mul_f32_e32 v84, 0x3d372713, v70
	v_mul_f32_e32 v86, 0x3d372713, v71
	v_mul_f32_e32 v88, 0x3d372713, v36
	v_mul_f32_e32 v90, 0x3d372713, v37
	v_mul_f32_e32 v92, 0x3d372713, v76
	v_mul_f32_e32 v94, 0x3d372713, v77
	v_mul_f32_e32 v96, 0x3d372713, v38
	v_mul_f32_e32 v98, 0x3d372713, v39
	v_mov_b32_e32 v85, v70
	v_mov_b32_e32 v87, v71
	v_pk_mul_f32 v[82:83], v[70:71], 0.5 op_sel_hi:[1,0]
	v_pk_add_f32 v[72:73], v[72:73], v[74:75]
	v_mov_b32_e32 v89, v36
	v_mov_b32_e32 v91, v37
	v_pk_mul_f32 v[74:75], v[36:37], 0.5 op_sel_hi:[1,0]
	v_mov_b32_e32 v93, v76
	v_mov_b32_e32 v95, v77
	v_pk_add_f32 v[78:79], v[78:79], v[80:81]
	v_mov_b32_e32 v97, v38
	v_mov_b32_e32 v99, v39
	v_pk_mul_f32 v[80:81], v[38:39], 0.5 op_sel_hi:[1,0]
	v_pk_add_f32 v[64:65], v[64:65], v[68:69]
	v_mul_f32_e32 v68, v84, v70
	v_mul_f32_e32 v69, v86, v71
	v_mul_f32_e32 v36, v88, v36
	v_mul_f32_e32 v37, v90, v37
	v_mul_f32_e32 v70, v92, v76
	v_mul_f32_e32 v71, v94, v77
	v_mul_f32_e32 v38, v96, v38
	v_mul_f32_e32 v39, v98, v39
	v_fmac_f32_e32 v85, v68, v85
	v_fmac_f32_e32 v87, v69, v87
	v_fmac_f32_e32 v89, v36, v89
	v_fmac_f32_e32 v91, v37, v91
	v_fmac_f32_e32 v93, v70, v93
	v_fmac_f32_e32 v95, v71, v95
	v_fmac_f32_e32 v97, v38, v97
	v_fmac_f32_e32 v99, v39, v99
	v_mul_f32_e32 v36, 0x3f4c422a, v85
	v_mul_f32_e32 v37, 0x3f4c422a, v87
	v_mul_f32_e32 v38, 0x3f4c422a, v89
	v_mul_f32_e32 v39, 0x3f4c422a, v91
	v_mul_f32_e32 v68, 0x3f4c422a, v93
	v_mul_f32_e32 v69, 0x3f4c422a, v95
	v_mul_f32_e32 v70, 0x3f4c422a, v97
	v_mul_f32_e32 v71, 0x3f4c422a, v99
	v_add_f32_e32 v36, v36, v36
	v_add_f32_e32 v37, v37, v37
	v_add_f32_e32 v38, v38, v38
	v_add_f32_e32 v39, v39, v39
	v_add_f32_e32 v68, v68, v68
	v_add_f32_e32 v69, v69, v69
	v_add_f32_e32 v70, v70, v70
	v_add_f32_e32 v71, v71, v71
	v_mul_f32_e32 v36, 0x3fb8aa3b, v36
	v_mul_f32_e32 v37, 0x3fb8aa3b, v37
	v_mul_f32_e32 v38, 0x3fb8aa3b, v38
	v_mul_f32_e32 v39, 0x3fb8aa3b, v39
	v_mul_f32_e32 v68, 0x3fb8aa3b, v68
	v_mul_f32_e32 v69, 0x3fb8aa3b, v69
	v_mul_f32_e32 v70, 0x3fb8aa3b, v70
	v_mul_f32_e32 v71, 0x3fb8aa3b, v71
	v_exp_f32_e32 v36, v36
	v_exp_f32_e32 v37, v37
	v_exp_f32_e32 v38, v38
	v_exp_f32_e32 v39, v39
	v_exp_f32_e32 v68, v68
	v_exp_f32_e32 v69, v69
	v_exp_f32_e32 v70, v70
	v_exp_f32_e32 v71, v71
	v_add_f32_e32 v36, 1.0, v36
	v_add_f32_e32 v37, 1.0, v37
	v_add_f32_e32 v38, 1.0, v38
	v_add_f32_e32 v39, 1.0, v39
	v_add_f32_e32 v68, 1.0, v68
	v_add_f32_e32 v69, 1.0, v69
	v_add_f32_e32 v70, 1.0, v70
	v_add_f32_e32 v71, 1.0, v71
	v_rcp_f32_e32 v36, v36
	v_rcp_f32_e32 v37, v37
	v_rcp_f32_e32 v38, v38
	v_rcp_f32_e32 v39, v39
	v_rcp_f32_e32 v68, v68
	v_rcp_f32_e32 v69, v69
	v_rcp_f32_e32 v70, v70
	v_rcp_f32_e32 v71, v71
	v_lshlrev_b32_e32 v62, 16, v117
	v_and_b32_e32 v63, 0xffff0000, v117
	v_lshlrev_b32_e32 v66, 16, v121
	v_and_b32_e32 v67, 0xffff0000, v121
	v_pk_fma_f32 v[36:37], v[36:37], 2.0, 1.0 op_sel_hi:[1,0,0] neg_lo:[1,0,0] neg_hi:[1,0,0]
	v_pk_fma_f32 v[38:39], v[38:39], 2.0, 1.0 op_sel_hi:[1,0,0] neg_lo:[1,0,0] neg_hi:[1,0,0]
	v_pk_fma_f32 v[68:69], v[68:69], 2.0, 1.0 op_sel_hi:[1,0,0] neg_lo:[1,0,0] neg_hi:[1,0,0]
	v_pk_fma_f32 v[70:71], v[70:71], 2.0, 1.0 op_sel_hi:[1,0,0] neg_lo:[1,0,0] neg_hi:[1,0,0]
	v_pk_add_f32 v[62:63], v[62:63], v[66:67]
	v_pk_mul_f32 v[66:67], v[76:77], 0.5 op_sel_hi:[1,0]
	v_pk_add_f32 v[36:37], v[36:37], 1.0 op_sel_hi:[1,0]
	v_pk_add_f32 v[38:39], v[38:39], 1.0 op_sel_hi:[1,0]
	v_pk_add_f32 v[68:69], v[68:69], 1.0 op_sel_hi:[1,0]
	v_pk_add_f32 v[70:71], v[70:71], 1.0 op_sel_hi:[1,0]
	v_pk_mul_f32 v[36:37], v[82:83], v[36:37]
	v_pk_mul_f32 v[38:39], v[74:75], v[38:39]
	v_pk_mul_f32 v[66:67], v[66:67], v[68:69]
	v_pk_mul_f32 v[68:69], v[80:81], v[70:71]
	v_pk_mul_f32 v[36:37], v[72:73], v[36:37]
	v_pk_mul_f32 v[38:39], v[62:63], v[38:39]
	v_pk_mul_f32 v[62:63], v[78:79], v[66:67]
	v_pk_mul_f32 v[64:65], v[64:65], v[68:69]
	v_cvt_pk_bf16_f32 v36, v36, v37
	v_cvt_pk_bf16_f32 v37, v38, v39
	v_cvt_pk_bf16_f32 v38, v62, v63
	v_cvt_pk_bf16_f32 v39, v64, v65
	global_store_dwordx4 v[40:41], v[36:39], off offset:16
	s_waitcnt vmcnt(9)
	v_lshlrev_b32_e32 v92, 16, v124
	v_and_b32_e32 v93, 0xffff0000, v124
	v_lshlrev_b32_e32 v94, 16, v125
	v_and_b32_e32 v95, 0xffff0000, v125
	v_lshlrev_b32_e32 v96, 16, v126
	v_and_b32_e32 v97, 0xffff0000, v126
	v_lshlrev_b32_e32 v98, 16, v127
	v_and_b32_e32 v99, 0xffff0000, v127
	s_waitcnt vmcnt(8)
	v_lshlrev_b32_e32 v100, 16, v128
	v_and_b32_e32 v101, 0xffff0000, v128
	v_lshlrev_b32_e32 v102, 16, v129
	v_and_b32_e32 v103, 0xffff0000, v129
	v_lshlrev_b32_e32 v104, 16, v130
	v_and_b32_e32 v105, 0xffff0000, v130
	v_lshlrev_b32_e32 v106, 16, v131
	v_and_b32_e32 v107, 0xffff0000, v131
	s_waitcnt vmcnt(7)
	v_and_b32_e32 v36, 0xffff0000, v135
	v_lshlrev_b32_e32 v37, 16, v135
	s_waitcnt vmcnt(6)
	v_and_b32_e32 v38, 0xffff0000, v139
	v_lshlrev_b32_e32 v39, 16, v139
	s_waitcnt vmcnt(5)
	v_lshlrev_b32_e32 v42, 16, v143
	v_and_b32_e32 v43, 0xffff0000, v143
	s_waitcnt vmcnt(4)
	v_lshlrev_b32_e32 v44, 16, v147
	v_and_b32_e32 v45, 0xffff0000, v147
	s_waitcnt vmcnt(3)
	v_lshlrev_b32_e32 v46, 16, v151
	v_and_b32_e32 v47, 0xffff0000, v151
	v_lshlrev_b32_e32 v48, 16, v142
	v_and_b32_e32 v49, 0xffff0000, v142
	v_lshlrev_b32_e32 v50, 16, v146
	v_and_b32_e32 v51, 0xffff0000, v146
	v_lshlrev_b32_e32 v52, 16, v150
	v_and_b32_e32 v53, 0xffff0000, v150
	v_lshlrev_b32_e32 v54, 16, v141
	v_and_b32_e32 v55, 0xffff0000, v141
	v_lshlrev_b32_e32 v56, 16, v145
	v_and_b32_e32 v57, 0xffff0000, v145
	v_lshlrev_b32_e32 v62, 16, v149
	v_and_b32_e32 v63, 0xffff0000, v149
	v_lshlrev_b32_e32 v64, 16, v140
	v_and_b32_e32 v65, 0xffff0000, v140
	v_lshlrev_b32_e32 v74, 16, v144
	v_and_b32_e32 v75, 0xffff0000, v144
	v_lshlrev_b32_e32 v76, 16, v148
	v_and_b32_e32 v77, 0xffff0000, v148
	v_lshlrev_b32_e32 v78, 16, v134
	v_and_b32_e32 v79, 0xffff0000, v134
	v_lshlrev_b32_e32 v68, 16, v138
	v_and_b32_e32 v69, 0xffff0000, v138
	s_waitcnt vmcnt(2)
	v_lshlrev_b32_e32 v72, 16, v154
	v_and_b32_e32 v73, 0xffff0000, v154
	v_lshlrev_b32_e32 v80, 16, v133
	v_and_b32_e32 v81, 0xffff0000, v133
	v_lshlrev_b32_e32 v82, 16, v137
	v_and_b32_e32 v83, 0xffff0000, v137
	v_lshlrev_b32_e32 v84, 16, v153
	v_and_b32_e32 v85, 0xffff0000, v153
	v_lshlrev_b32_e32 v90, 16, v132
	v_and_b32_e32 v91, 0xffff0000, v132
	v_lshlrev_b32_e32 v66, 16, v136
	v_and_b32_e32 v67, 0xffff0000, v136
	v_lshlrev_b32_e32 v70, 16, v152
	v_and_b32_e32 v71, 0xffff0000, v152
	v_lshlrev_b32_e32 v86, 16, v155
	v_and_b32_e32 v87, 0xffff0000, v155
	v_mul_f32_e32 v88, 0xbfb8aa3b, v92
	v_mul_f32_e32 v89, 0xbfb8aa3b, v93
	v_mul_f32_e32 v92, 0xbfb8aa3b, v94
	v_mul_f32_e32 v93, 0xbfb8aa3b, v95
	v_mul_f32_e32 v94, 0xbfb8aa3b, v96
	v_mul_f32_e32 v95, 0xbfb8aa3b, v97
	v_mul_f32_e32 v96, 0xbfb8aa3b, v98
	v_mul_f32_e32 v97, 0xbfb8aa3b, v99
	v_mul_f32_e32 v98, 0xbfb8aa3b, v100
	v_mul_f32_e32 v99, 0xbfb8aa3b, v101
	v_pk_add_f32 v[36:37], v[36:37], v[38:39]
	v_pk_add_f32 v[38:39], v[42:43], v[44:45]
	v_pk_add_f32 v[42:43], v[48:49], v[50:51]
	v_pk_add_f32 v[48:49], v[64:65], v[74:75]
	v_exp_f32_e32 v64, v88
	v_exp_f32_e32 v65, v89
	v_pk_add_f32 v[44:45], v[54:55], v[56:57]
	v_pk_add_f32 v[50:51], v[78:79], v[68:69]
	v_pk_add_f32 v[56:57], v[90:91], v[66:67]
	v_exp_f32_e32 v66, v92
	v_exp_f32_e32 v67, v93
	v_exp_f32_e32 v78, v98
	v_exp_f32_e32 v79, v99
	v_exp_f32_e32 v74, v96
	v_exp_f32_e32 v75, v97
	v_exp_f32_e32 v68, v94
	v_exp_f32_e32 v69, v95
	v_add_f32_e32 v64, 1.0, v64
	v_add_f32_e32 v65, 1.0, v65
	v_add_f32_e32 v66, 1.0, v66
	v_add_f32_e32 v67, 1.0, v67
	v_add_f32_e32 v78, 1.0, v78
	v_add_f32_e32 v79, 1.0, v79
	v_rcp_f32_e32 v64, v64
	v_rcp_f32_e32 v65, v65
	v_add_f32_e32 v74, 1.0, v74
	v_add_f32_e32 v75, 1.0, v75
	v_rcp_f32_e32 v66, v66
	v_rcp_f32_e32 v67, v67
	v_rcp_f32_e32 v78, v78
	v_rcp_f32_e32 v79, v79
	v_mul_f32_e32 v100, 0xbfb8aa3b, v102
	v_mul_f32_e32 v101, 0xbfb8aa3b, v103
	v_mul_f32_e32 v102, 0xbfb8aa3b, v104
	v_mul_f32_e32 v103, 0xbfb8aa3b, v105
	v_mul_f32_e32 v104, 0xbfb8aa3b, v106
	v_mul_f32_e32 v105, 0xbfb8aa3b, v107
	v_add_f32_e32 v68, 1.0, v68
	v_add_f32_e32 v69, 1.0, v69
	v_rcp_f32_e32 v74, v74
	v_rcp_f32_e32 v75, v75
	v_pk_add_f32 v[54:55], v[80:81], v[82:83]
	v_exp_f32_e32 v82, v102
	v_exp_f32_e32 v83, v103
	v_exp_f32_e32 v88, v104
	v_exp_f32_e32 v89, v105
	v_rcp_f32_e32 v68, v68
	v_rcp_f32_e32 v69, v69
	v_exp_f32_e32 v80, v100
	v_exp_f32_e32 v81, v101
	v_pk_mul_f32 v[48:49], v[48:49], v[64:65]
	v_pk_mul_f32 v[44:45], v[44:45], v[66:67]
	v_pk_mul_f32 v[56:57], v[56:57], v[78:79]
	v_pk_mul_f32 v[78:79], v[48:49], v[48:49]
	v_pk_mul_f32 v[38:39], v[38:39], v[74:75]
	v_pk_mul_f32 v[74:75], v[44:45], v[44:45]
	v_add_f32_e32 v78, v78, v79
	v_add_f32_e32 v90, 1.0, v82
	v_add_f32_e32 v91, 1.0, v83
	v_add_f32_e32 v82, 1.0, v88
	v_add_f32_e32 v88, 1.0, v89
	v_pk_mul_f32 v[42:43], v[42:43], v[68:69]
	v_add_f32_e32 v74, v74, v78
	v_add_f32_e32 v80, 1.0, v80
	v_add_f32_e32 v81, 1.0, v81
	v_rcp_f32_e32 v83, v82
	v_rcp_f32_e32 v82, v88
	v_rcp_f32_e32 v88, v90
	v_rcp_f32_e32 v89, v91
	v_pk_mul_f32 v[68:69], v[42:43], v[42:43]
	v_add_f32_e32 v74, v75, v74
	v_rcp_f32_e32 v80, v80
	v_rcp_f32_e32 v81, v81
	v_add_f32_e32 v68, v68, v74
	v_pk_mul_f32 v[66:67], v[38:39], v[38:39]
	v_add_f32_e32 v68, v69, v68
	v_add_f32_e32 v66, v66, v68
	v_pk_mul_f32 v[50:51], v[50:51], v[88:89]
	v_pk_mul_f32 v[88:89], v[56:57], v[56:57]
	v_add_f32_e32 v66, v67, v66
	v_pk_mul_f32 v[54:55], v[54:55], v[80:81]
	v_add_f32_e32 v66, v88, v66
	v_pk_mul_f32 v[36:37], v[36:37], v[82:83]
	v_pk_mul_f32 v[82:83], v[54:55], v[54:55]
	v_add_f32_e32 v66, v89, v66
	v_add_f32_e32 v66, v82, v66
	v_pk_mul_f32 v[80:81], v[50:51], v[50:51]
	v_add_f32_e32 v66, v83, v66
	v_add_f32_e32 v66, v80, v66
	v_pk_mul_f32 v[64:65], v[36:37], v[36:37]
	v_add_f32_e32 v66, v81, v66
	v_add_f32_e32 v65, v65, v66
	v_add_f32_e32 v64, v64, v65
	ds_bpermute_b32 v65, v1, v64
	s_waitcnt lgkmcnt(0)
	v_add_f32_e32 v64, v64, v65
	ds_bpermute_b32 v65, v58, v64
	s_waitcnt lgkmcnt(0)
	v_add_f32_e32 v64, v64, v65
	ds_bpermute_b32 v65, v59, v64
	s_waitcnt lgkmcnt(0)
	v_add_f32_e32 v64, v64, v65
	ds_bpermute_b32 v65, v60, v64
	s_waitcnt lgkmcnt(0)
	v_add_f32_e32 v64, v64, v65
	v_fmamk_f32 v64, v64, 0x3b800000, v61
	v_mul_f32_e32 v65, 0x4b800000, v64
	v_cmp_gt_f32_e32 vcc, s44, v64
	s_nop 1
	v_cndmask_b32_e32 v64, v64, v65, vcc
	v_rsq_f32_e32 v64, v64
	s_nop 0
	v_mul_f32_e32 v65, 0x45800000, v64
	v_cndmask_b32_e32 v64, v64, v65, vcc
	v_pk_mul_f32 v[48:49], v[48:49], v[64:65] op_sel_hi:[1,0]
	v_pk_mul_f32 v[44:45], v[44:45], v[64:65] op_sel_hi:[1,0]
	v_pk_mul_f32 v[42:43], v[42:43], v[64:65] op_sel_hi:[1,0]
	v_pk_mul_f32 v[38:39], v[38:39], v[64:65] op_sel_hi:[1,0]
	v_pk_mul_f32 v[56:57], v[56:57], v[64:65] op_sel_hi:[1,0]
	v_pk_mul_f32 v[54:55], v[54:55], v[64:65] op_sel_hi:[1,0]
	v_pk_mul_f32 v[50:51], v[50:51], v[64:65] op_sel_hi:[1,0]
	v_pk_mul_f32 v[36:37], v[36:37], v[64:65] op_sel_hi:[1,0]
	v_pk_mul_f32 v[48:49], v[14:15], v[48:49]
	v_pk_mul_f32 v[44:45], v[16:17], v[44:45]
	v_pk_mul_f32 v[42:43], v[10:11], v[42:43]
	v_pk_mul_f32 v[38:39], v[12:13], v[38:39]
	v_pk_mul_f32 v[56:57], v[6:7], v[56:57]
	v_pk_mul_f32 v[54:55], v[8:9], v[54:55]
	v_pk_mul_f32 v[50:51], v[2:3], v[50:51]
	v_pk_mul_f32 v[36:37], v[4:5], v[36:37] op_sel:[0,1] op_sel_hi:[1,0]
	v_pk_fma_f32 v[48:49], v[30:31], v[76:77], v[48:49]
	v_pk_fma_f32 v[44:45], v[32:33], v[62:63], v[44:45]
	v_pk_fma_f32 v[42:43], v[26:27], v[52:53], v[42:43]
	v_pk_fma_f32 v[46:47], v[28:29], v[46:47], v[38:39]
	v_pk_fma_f32 v[52:53], v[22:23], v[70:71], v[56:57]
	v_pk_fma_f32 v[54:55], v[24:25], v[84:85], v[54:55]
	v_pk_fma_f32 v[50:51], v[18:19], v[72:73], v[50:51]
	v_pk_fma_f32 v[56:57], v[20:21], v[86:87], v[36:37]
	v_cvt_pk_bf16_f32 v36, v48, v49
	v_cvt_pk_bf16_f32 v37, v44, v45
	v_cvt_pk_bf16_f32 v38, v42, v43
	v_cvt_pk_bf16_f32 v39, v46, v47
	v_cvt_pk_bf16_f32 v42, v52, v53
	v_cvt_pk_bf16_f32 v43, v54, v55
	v_cvt_pk_bf16_f32 v44, v50, v51
	v_cvt_pk_bf16_f32 v45, v56, v57
	global_store_dwordx4 v[40:41], v[36:39], off offset:2048
	global_store_dwordx4 v[40:41], v[42:45], off offset:2064
	s_cbranch_scc1 .LBB0_1118
